# P6 out-proj epilogue: residual (HN) row loads prefetched 3 steps ahead into dead fragment VGPRs, counted vmcnt instead of vmcnt(0) ladder
# speedup vs baseline: 1.0131x; 1.0131x over previous
; __device__ __forceinline__ unsigned pk2(float lo, float hi) { const f32v2 v = {lo, hi}; return __builtin_bit_cast(unsigned, __builtin_convertvector(v, bf16v2)); }
;     __device__ __forceinline__ void operator()(const f32x4 (&acc)[2][2][4][2], const pg8::Unit& u, int wr, int wc, int fr, int fq, int ui) const {
;     ...
;         const int row0 = u.pm * 256 + wr * 64 + fr, col0 = u.pn * 256 + wc * 32 + 8 * fq;
;         const float* g1 = MOD + ((u.pm * 256) / SEQ) * (6 * D) + 2 * D;
;         f32x4 gv[2][2];
; #pragma unroll
;         for (int bj = 0; bj < 2; ++bj)
; #pragma unroll
;             for (int n = 0; n < 2; ++n) gv[bj][n] = *(const f32x4*)(g1 + col0 + bj * 128 + 4 * n);
; #pragma unroll
;         for (int ai = 0; ai < 2; ++ai)
; #pragma unroll
;             for (int m = 0; m < 4; ++m) { const size_t ro = (size_t)(row0 + ai * 128 + m * 16) * D + col0;
; #pragma unroll
;                 for (int bj = 0; bj < 2; ++bj) { const u32x4 h = *(const u32x4*)(HN + ro + bj * 128); const f32x4 a0 = acc[ai][bj][m][0], a1 = acc[ai][bj][m][1], g0 = gv[bj][0], g1v = gv[bj][1];
;                     u32x4 o; o.x = pk2(ALPHA * bflo(h.x) + g0.x * a0.x, ALPHA * bfhi(h.x) + g0.y * a0.y); o.y = pk2(ALPHA * bflo(h.y) + g0.z * a0.z, ALPHA * bfhi(h.y) + g0.w * a0.w);
;                     o.z = pk2(ALPHA * bflo(h.z) + g1v.x * a1.x, ALPHA * bfhi(h.z) + g1v.y * a1.y); o.w = pk2(ALPHA * bflo(h.w) + g1v.z * a1.z, ALPHA * bfhi(h.w) + g1v.w * a1.w);
;                     *(u32x4*)(Z + ro + bj * 128) = o; } }
.LBB0_687:
	v_mov_b32_e32 v120, v223
	v_mov_b32_e32 v118, v224
	s_lshl_b32 s8, s54, 8
	s_add_i32 s8, s8, s47
	v_add_u32_e32 v120, s8, v120
	s_ashr_i32 s8, s54, 31
	s_lshr_b32 s8, s8, 28
	s_add_i32 s8, s54, s8
	s_lshl_b32 s9, s55, 8
	s_lshr_b32 s8, s8, 4
	s_or_b32 s9, s9, s48
	s_mulk_i32 s8, 0x3000
	v_lshl_add_u32 v118, v118, 3, s9
	s_ashr_i32 s9, s8, 31
	s_lshl_b64 s[8:9], s[8:9], 2
	v_ashrrev_i32_e32 v121, 31, v120
	s_add_u32 s8, s96, s8
	v_ashrrev_i32_e32 v119, 31, v118
	v_lshlrev_b64 v[120:121], 11, v[120:121]
	s_addc_u32 s9, s97, s9
	v_lshl_add_u64 v[120:121], v[120:121], 0, v[118:119]
	v_lshl_add_u64 v[122:123], v[118:119], 2, s[8:9]
	s_movk_i32 s8, 0x4000
	v_lshlrev_b64 v[146:147], 1, v[120:121]
	v_add_co_u32_e32 v118, vcc, s8, v122
	v_lshl_add_u64 v[120:121], s[12:13], 0, v[146:147]
	s_nop 0
	v_addc_co_u32_e32 v119, vcc, 0, v123, vcc
	s_mov_b64 s[8:9], 0x4000
	global_load_dwordx4 v[148:151], v[120:121], off
	global_load_dwordx4 v[152:155], v[120:121], off offset:256
	v_lshl_add_u64 v[122:123], v[122:123], 0, s[8:9]
	global_load_dwordx4 v[118:121], v[118:119], off
	s_nop 0
	global_load_dwordx4 v[126:129], v[122:123], off offset:16
	global_load_dwordx4 v[130:133], v[122:123], off offset:512
	s_nop 0
	global_load_dwordx4 v[122:125], v[122:123], off offset:528
	v_add_u32_e32 v170, 0x10000, v146
	global_load_dwordx4 v[170:173], v170, s[12:13]
	v_add_u32_e32 v174, 0x10000, v146
	global_load_dwordx4 v[174:177], v174, s[12:13] offset:256
	v_add_u32_e32 v178, 0x20000, v146
	global_load_dwordx4 v[178:181], v178, s[12:13]
	v_add_u32_e32 v182, 0x20000, v146
	global_load_dwordx4 v[182:185], v182, s[12:13] offset:256
	v_add_u32_e32 v186, 0x30000, v146
	global_load_dwordx4 v[186:189], v186, s[12:13]
	v_add_u32_e32 v190, 0x30000, v146
	global_load_dwordx4 v[190:193], v190, s[12:13] offset:256
	s_mov_b64 s[8:9], 0x10000
	v_lshl_add_u64 v[156:157], s[14:15], 0, v[146:147]
	v_lshl_add_u64 v[158:159], v[146:147], 0, s[8:9]
	v_lshl_add_u64 v[160:161], s[12:13], 0, v[158:159]
	s_mov_b64 s[8:9], 0x20000
	s_and_b64 vcc, exec, s[6:7]
	s_mov_b64 s[6:7], -1
	s_waitcnt vmcnt(6)
	v_lshlrev_b32_e32 v162, 16, v148
	v_and_b32_e32 v163, 0xffff0000, v148
	v_lshlrev_b32_e32 v148, 16, v149
	v_and_b32_e32 v149, 0xffff0000, v149
	v_lshlrev_b32_e32 v164, 16, v150
	v_and_b32_e32 v165, 0xffff0000, v150
	v_lshlrev_b32_e32 v150, 16, v151
	v_and_b32_e32 v151, 0xffff0000, v151
	v_pk_mul_f32 v[144:145], v[144:145], v[120:121]
	v_pk_mul_f32 v[142:143], v[142:143], v[118:119]
	v_pk_mul_f32 v[140:141], v[140:141], v[128:129]
	v_pk_mul_f32 v[138:139], v[138:139], v[126:127]
	v_lshlrev_b32_e32 v166, 16, v152
	v_and_b32_e32 v167, 0xffff0000, v152
	v_lshlrev_b32_e32 v152, 16, v153
	v_and_b32_e32 v153, 0xffff0000, v153
	v_lshlrev_b32_e32 v168, 16, v154
	v_and_b32_e32 v169, 0xffff0000, v154
	v_lshlrev_b32_e32 v154, 16, v155
	v_and_b32_e32 v155, 0xffff0000, v155
	v_pk_mul_f32 v[136:137], v[136:137], v[132:133]
	v_pk_mul_f32 v[134:135], v[134:135], v[130:131]
	v_pk_mul_f32 v[116:117], v[116:117], v[124:125]
	v_pk_mul_f32 v[114:115], v[114:115], v[122:123]
	v_pk_fma_f32 v[142:143], v[162:163], s[26:27], v[142:143] op_sel_hi:[1,0,1]
	v_pk_fma_f32 v[144:145], v[148:149], s[26:27], v[144:145] op_sel_hi:[1,0,1]
	v_pk_fma_f32 v[138:139], v[164:165], s[26:27], v[138:139] op_sel_hi:[1,0,1]
	v_pk_fma_f32 v[140:141], v[150:151], s[26:27], v[140:141] op_sel_hi:[1,0,1]
	v_pk_fma_f32 v[134:135], v[166:167], s[26:27], v[134:135] op_sel_hi:[1,0,1]
	v_pk_fma_f32 v[136:137], v[152:153], s[26:27], v[136:137] op_sel_hi:[1,0,1]
	v_pk_fma_f32 v[148:149], v[168:169], s[26:27], v[114:115] op_sel_hi:[1,0,1]
	v_pk_fma_f32 v[150:151], v[154:155], s[26:27], v[116:117] op_sel_hi:[1,0,1]
	v_cvt_pk_bf16_f32 v114, v142, v143
	v_cvt_pk_bf16_f32 v115, v144, v145
	v_cvt_pk_bf16_f32 v116, v138, v139
	v_cvt_pk_bf16_f32 v117, v140, v141
	v_cvt_pk_bf16_f32 v134, v134, v135
	v_cvt_pk_bf16_f32 v135, v136, v137
	v_cvt_pk_bf16_f32 v136, v148, v149
	v_cvt_pk_bf16_f32 v137, v150, v151
	global_store_dwordx4 v[156:157], v[114:117], off
	global_store_dwordx4 v[156:157], v[134:137], off offset:256
	v_pk_mul_f32 v[112:113], v[112:113], v[120:121]
	v_pk_mul_f32 v[110:111], v[110:111], v[118:119]
	v_pk_mul_f32 v[108:109], v[108:109], v[128:129]
	v_pk_mul_f32 v[106:107], v[106:107], v[126:127]
	v_pk_mul_f32 v[104:105], v[104:105], v[132:133]
	v_pk_mul_f32 v[102:103], v[102:103], v[130:131]
	v_pk_mul_f32 v[100:101], v[100:101], v[124:125]
	v_pk_mul_f32 v[98:99], v[98:99], v[122:123]
	v_lshl_add_u64 v[138:139], v[146:147], 0, s[8:9]
	v_lshl_add_u64 v[140:141], s[14:15], 0, v[158:159]
	v_lshl_add_u64 v[142:143], s[12:13], 0, v[138:139]
	v_pk_mul_f32 v[96:97], v[96:97], v[120:121]
	v_pk_mul_f32 v[94:95], v[94:95], v[118:119]
	v_pk_mul_f32 v[92:93], v[92:93], v[128:129]
	v_pk_mul_f32 v[90:91], v[90:91], v[126:127]
	s_mov_b64 s[8:9], 0x30000
	v_pk_mul_f32 v[88:89], v[88:89], v[132:133]
	v_pk_mul_f32 v[86:87], v[86:87], v[130:131]
	v_pk_mul_f32 v[84:85], v[84:85], v[124:125]
	v_pk_mul_f32 v[82:83], v[82:83], v[122:123]
	v_pk_mul_f32 v[80:81], v[80:81], v[120:121]
	v_pk_mul_f32 v[78:79], v[78:79], v[118:119]
	v_pk_mul_f32 v[76:77], v[76:77], v[128:129]
	v_pk_mul_f32 v[74:75], v[74:75], v[126:127]
	v_pk_mul_f32 v[72:73], v[72:73], v[132:133]
	v_pk_mul_f32 v[70:71], v[70:71], v[130:131]
	v_pk_mul_f32 v[68:69], v[68:69], v[124:125]
	v_pk_mul_f32 v[66:67], v[66:67], v[122:123]
	v_pk_mul_f32 v[64:65], v[64:65], v[120:121]
	v_pk_mul_f32 v[62:63], v[62:63], v[118:119]
	v_pk_mul_f32 v[60:61], v[60:61], v[128:129]
	v_pk_mul_f32 v[58:59], v[58:59], v[126:127]
	v_pk_mul_f32 v[56:57], v[56:57], v[132:133]
	v_pk_mul_f32 v[54:55], v[54:55], v[130:131]
	v_pk_mul_f32 v[52:53], v[52:53], v[124:125]
	v_pk_mul_f32 v[50:51], v[50:51], v[122:123]
	v_pk_mul_f32 v[48:49], v[48:49], v[120:121]
	v_pk_mul_f32 v[46:47], v[46:47], v[118:119]
	v_pk_mul_f32 v[44:45], v[44:45], v[128:129]
	v_pk_mul_f32 v[42:43], v[42:43], v[126:127]
	v_pk_mul_f32 v[40:41], v[40:41], v[132:133]
	v_pk_mul_f32 v[38:39], v[38:39], v[130:131]
	v_pk_mul_f32 v[36:37], v[36:37], v[124:125]
	v_pk_mul_f32 v[34:35], v[34:35], v[122:123]
	v_pk_mul_f32 v[32:33], v[32:33], v[120:121]
	v_pk_mul_f32 v[30:31], v[30:31], v[118:119]
	v_pk_mul_f32 v[28:29], v[28:29], v[128:129]
	v_pk_mul_f32 v[26:27], v[26:27], v[126:127]
	v_pk_mul_f32 v[24:25], v[24:25], v[132:133]
	v_pk_mul_f32 v[22:23], v[22:23], v[130:131]
	v_pk_mul_f32 v[20:21], v[20:21], v[124:125]
	v_pk_mul_f32 v[18:19], v[18:19], v[122:123]
	v_pk_mul_f32 v[16:17], v[16:17], v[120:121]
	v_pk_mul_f32 v[14:15], v[14:15], v[118:119]
	v_pk_mul_f32 v[12:13], v[12:13], v[128:129]
	v_pk_mul_f32 v[10:11], v[10:11], v[126:127]
	v_pk_mul_f32 v[8:9], v[8:9], v[132:133]
	v_pk_mul_f32 v[6:7], v[6:7], v[130:131]
	v_pk_mul_f32 v[4:5], v[4:5], v[124:125]
	v_pk_mul_f32 v[2:3], v[2:3], v[122:123]
	s_waitcnt vmcnt(6)
; __device__ __forceinline__ unsigned pk2(float lo, float hi) { const f32v2 v = {lo, hi}; return __builtin_bit_cast(unsigned, __builtin_convertvector(v, bf16v2)); }
;     __device__ __forceinline__ void operator()(const f32x4 (&acc)[2][2][4][2], const pg8::Unit& u, int wr, int wc, int fr, int fq, int ui) const {
;     ...
;         for (int ai = 0; ai < 2; ++ai)
; #pragma unroll
;             for (int m = 0; m < 4; ++m) { const size_t ro = (size_t)(row0 + ai * 128 + m * 16) * D + col0;
; #pragma unroll
;                 for (int bj = 0; bj < 2; ++bj) { const u32x4 h = *(const u32x4*)(HN + ro + bj * 128); const f32x4 a0 = acc[ai][bj][m][0], a1 = acc[ai][bj][m][1], g0 = gv[bj][0], g1v = gv[bj][1];
;                     u32x4 o; o.x = pk2(ALPHA * bflo(h.x) + g0.x * a0.x, ALPHA * bfhi(h.x) + g0.y * a0.y); o.y = pk2(ALPHA * bflo(h.y) + g0.z * a0.z, ALPHA * bfhi(h.y) + g0.w * a0.w);
;                     o.z = pk2(ALPHA * bflo(h.z) + g1v.x * a1.x, ALPHA * bfhi(h.z) + g1v.y * a1.y); o.w = pk2(ALPHA * bflo(h.w) + g1v.z * a1.z, ALPHA * bfhi(h.w) + g1v.w * a1.w);
;                     *(u32x4*)(Z + ro + bj * 128) = o; } }
	v_lshlrev_b32_e32 v144, 16, v170
	v_and_b32_e32 v145, 0xffff0000, v170
	v_lshlrev_b32_e32 v114, 16, v171
	v_and_b32_e32 v115, 0xffff0000, v171
	v_lshlrev_b32_e32 v148, 16, v172
	v_and_b32_e32 v149, 0xffff0000, v172
	v_lshlrev_b32_e32 v116, 16, v173
	v_and_b32_e32 v117, 0xffff0000, v173
	s_waitcnt vmcnt(6)
	v_lshlrev_b32_e32 v150, 16, v174
	v_and_b32_e32 v151, 0xffff0000, v174
	v_lshlrev_b32_e32 v134, 16, v175
	v_and_b32_e32 v135, 0xffff0000, v175
	v_lshlrev_b32_e32 v152, 16, v176
	v_and_b32_e32 v153, 0xffff0000, v176
	v_lshlrev_b32_e32 v136, 16, v177
	v_and_b32_e32 v137, 0xffff0000, v177
	v_pk_fma_f32 v[110:111], v[144:145], s[26:27], v[110:111] op_sel_hi:[1,0,1]
	v_pk_fma_f32 v[112:113], v[114:115], s[26:27], v[112:113] op_sel_hi:[1,0,1]
	v_pk_fma_f32 v[106:107], v[148:149], s[26:27], v[106:107] op_sel_hi:[1,0,1]
	v_pk_fma_f32 v[108:109], v[116:117], s[26:27], v[108:109] op_sel_hi:[1,0,1]
	v_pk_fma_f32 v[102:103], v[150:151], s[26:27], v[102:103] op_sel_hi:[1,0,1]
	v_pk_fma_f32 v[104:105], v[134:135], s[26:27], v[104:105] op_sel_hi:[1,0,1]
	v_pk_fma_f32 v[114:115], v[152:153], s[26:27], v[98:99] op_sel_hi:[1,0,1]
	v_pk_fma_f32 v[116:117], v[136:137], s[26:27], v[100:101] op_sel_hi:[1,0,1]
	v_cvt_pk_bf16_f32 v98, v110, v111
	v_cvt_pk_bf16_f32 v99, v112, v113
	v_cvt_pk_bf16_f32 v100, v106, v107
	v_cvt_pk_bf16_f32 v101, v108, v109
	v_cvt_pk_bf16_f32 v102, v102, v103
	v_cvt_pk_bf16_f32 v103, v104, v105
	v_cvt_pk_bf16_f32 v104, v114, v115
	v_cvt_pk_bf16_f32 v105, v116, v117
	global_store_dwordx4 v[140:141], v[98:101], off
	global_store_dwordx4 v[140:141], v[102:105], off offset:256
	v_add_u32_e32 v170, 0x80000, v146
	global_load_dwordx4 v[170:173], v170, s[12:13]
	v_add_u32_e32 v174, 0x80000, v146
	global_load_dwordx4 v[174:177], v174, s[12:13] offset:256
	v_lshl_add_u64 v[106:107], v[146:147], 0, s[8:9]
	v_lshl_add_u64 v[108:109], s[14:15], 0, v[138:139]
	v_lshl_add_u64 v[110:111], s[12:13], 0, v[106:107]
	s_mov_b64 s[8:9], 0x80000
	s_waitcnt vmcnt(8)
	v_lshlrev_b32_e32 v112, 16, v178
	v_and_b32_e32 v113, 0xffff0000, v178
	v_lshlrev_b32_e32 v98, 16, v179
	v_and_b32_e32 v99, 0xffff0000, v179
	v_lshlrev_b32_e32 v114, 16, v180
	v_and_b32_e32 v115, 0xffff0000, v180
	v_lshlrev_b32_e32 v100, 16, v181
	v_and_b32_e32 v101, 0xffff0000, v181
	s_waitcnt vmcnt(8)
	v_lshlrev_b32_e32 v116, 16, v182
	v_and_b32_e32 v117, 0xffff0000, v182
	v_lshlrev_b32_e32 v102, 16, v183
	v_and_b32_e32 v103, 0xffff0000, v183
	v_lshlrev_b32_e32 v134, 16, v184
	v_and_b32_e32 v135, 0xffff0000, v184
	v_lshlrev_b32_e32 v104, 16, v185
	v_and_b32_e32 v105, 0xffff0000, v185
	v_pk_fma_f32 v[94:95], v[112:113], s[26:27], v[94:95] op_sel_hi:[1,0,1]
	v_pk_fma_f32 v[96:97], v[98:99], s[26:27], v[96:97] op_sel_hi:[1,0,1]
	v_pk_fma_f32 v[90:91], v[114:115], s[26:27], v[90:91] op_sel_hi:[1,0,1]
	v_pk_fma_f32 v[92:93], v[100:101], s[26:27], v[92:93] op_sel_hi:[1,0,1]
	v_pk_fma_f32 v[86:87], v[116:117], s[26:27], v[86:87] op_sel_hi:[1,0,1]
	v_pk_fma_f32 v[88:89], v[102:103], s[26:27], v[88:89] op_sel_hi:[1,0,1]
	v_pk_fma_f32 v[98:99], v[134:135], s[26:27], v[82:83] op_sel_hi:[1,0,1]
	v_pk_fma_f32 v[100:101], v[104:105], s[26:27], v[84:85] op_sel_hi:[1,0,1]
	v_cvt_pk_bf16_f32 v82, v94, v95
	v_cvt_pk_bf16_f32 v83, v96, v97
	v_cvt_pk_bf16_f32 v84, v90, v91
	v_cvt_pk_bf16_f32 v85, v92, v93
	v_cvt_pk_bf16_f32 v86, v86, v87
	v_cvt_pk_bf16_f32 v87, v88, v89
	v_cvt_pk_bf16_f32 v88, v98, v99
	v_cvt_pk_bf16_f32 v89, v100, v101
	global_store_dwordx4 v[108:109], v[82:85], off
	global_store_dwordx4 v[108:109], v[86:89], off offset:256
	v_add_u32_e32 v178, 0x90000, v146
	global_load_dwordx4 v[178:181], v178, s[12:13]
	v_add_u32_e32 v182, 0x90000, v146
	global_load_dwordx4 v[182:185], v182, s[12:13] offset:256
	v_lshl_add_u64 v[90:91], v[146:147], 0, s[8:9]
	v_lshl_add_u64 v[92:93], s[14:15], 0, v[106:107]
	v_lshl_add_u64 v[94:95], s[12:13], 0, v[90:91]
	s_mov_b64 s[8:9], 0x90000
	s_waitcnt vmcnt(10)
	v_lshlrev_b32_e32 v96, 16, v186
	v_and_b32_e32 v97, 0xffff0000, v186
	v_lshlrev_b32_e32 v82, 16, v187
	v_and_b32_e32 v83, 0xffff0000, v187
	v_lshlrev_b32_e32 v98, 16, v188
	v_and_b32_e32 v99, 0xffff0000, v188
	v_lshlrev_b32_e32 v84, 16, v189
	v_and_b32_e32 v85, 0xffff0000, v189
	s_waitcnt vmcnt(10)
	v_lshlrev_b32_e32 v100, 16, v190
	v_and_b32_e32 v101, 0xffff0000, v190
	v_lshlrev_b32_e32 v86, 16, v191
	v_and_b32_e32 v87, 0xffff0000, v191
	v_lshlrev_b32_e32 v102, 16, v192
	v_and_b32_e32 v103, 0xffff0000, v192
	v_lshlrev_b32_e32 v88, 16, v193
	v_and_b32_e32 v89, 0xffff0000, v193
	v_pk_fma_f32 v[78:79], v[96:97], s[26:27], v[78:79] op_sel_hi:[1,0,1]
	v_pk_fma_f32 v[80:81], v[82:83], s[26:27], v[80:81] op_sel_hi:[1,0,1]
	v_pk_fma_f32 v[74:75], v[98:99], s[26:27], v[74:75] op_sel_hi:[1,0,1]
	v_pk_fma_f32 v[76:77], v[84:85], s[26:27], v[76:77] op_sel_hi:[1,0,1]
	v_pk_fma_f32 v[70:71], v[100:101], s[26:27], v[70:71] op_sel_hi:[1,0,1]
	v_pk_fma_f32 v[72:73], v[86:87], s[26:27], v[72:73] op_sel_hi:[1,0,1]
	v_pk_fma_f32 v[82:83], v[102:103], s[26:27], v[66:67] op_sel_hi:[1,0,1]
	v_pk_fma_f32 v[84:85], v[88:89], s[26:27], v[68:69] op_sel_hi:[1,0,1]
	v_cvt_pk_bf16_f32 v66, v78, v79
	v_cvt_pk_bf16_f32 v67, v80, v81
	v_cvt_pk_bf16_f32 v68, v74, v75
	v_cvt_pk_bf16_f32 v69, v76, v77
	v_cvt_pk_bf16_f32 v70, v70, v71
	v_cvt_pk_bf16_f32 v71, v72, v73
	v_cvt_pk_bf16_f32 v72, v82, v83
	v_cvt_pk_bf16_f32 v73, v84, v85
	global_store_dwordx4 v[92:93], v[66:69], off
	global_store_dwordx4 v[92:93], v[70:73], off offset:256
	v_add_u32_e32 v186, 0xa0000, v146
	global_load_dwordx4 v[186:189], v186, s[12:13]
	v_add_u32_e32 v190, 0xa0000, v146
	global_load_dwordx4 v[190:193], v190, s[12:13] offset:256
	v_lshl_add_u64 v[74:75], v[146:147], 0, s[8:9]
	v_lshl_add_u64 v[76:77], s[14:15], 0, v[90:91]
	v_lshl_add_u64 v[78:79], s[12:13], 0, v[74:75]
	s_mov_b64 s[8:9], 0xa0000
	s_waitcnt vmcnt(8)
; __device__ __forceinline__ unsigned pk2(float lo, float hi) { const f32v2 v = {lo, hi}; return __builtin_bit_cast(unsigned, __builtin_convertvector(v, bf16v2)); }
;     __device__ __forceinline__ void operator()(const f32x4 (&acc)[2][2][4][2], const pg8::Unit& u, int wr, int wc, int fr, int fq, int ui) const {
;     ...
;         for (int ai = 0; ai < 2; ++ai)
; #pragma unroll
;             for (int m = 0; m < 4; ++m) { const size_t ro = (size_t)(row0 + ai * 128 + m * 16) * D + col0;
; #pragma unroll
;                 for (int bj = 0; bj < 2; ++bj) { const u32x4 h = *(const u32x4*)(HN + ro + bj * 128); const f32x4 a0 = acc[ai][bj][m][0], a1 = acc[ai][bj][m][1], g0 = gv[bj][0], g1v = gv[bj][1];
;                     u32x4 o; o.x = pk2(ALPHA * bflo(h.x) + g0.x * a0.x, ALPHA * bfhi(h.x) + g0.y * a0.y); o.y = pk2(ALPHA * bflo(h.y) + g0.z * a0.z, ALPHA * bfhi(h.y) + g0.w * a0.w);
;                     o.z = pk2(ALPHA * bflo(h.z) + g1v.x * a1.x, ALPHA * bfhi(h.z) + g1v.y * a1.y); o.w = pk2(ALPHA * bflo(h.w) + g1v.z * a1.z, ALPHA * bfhi(h.w) + g1v.w * a1.w);
;                     *(u32x4*)(Z + ro + bj * 128) = o; } }
	v_lshlrev_b32_e32 v80, 16, v170
	v_and_b32_e32 v81, 0xffff0000, v170
	v_lshlrev_b32_e32 v66, 16, v171
	v_and_b32_e32 v67, 0xffff0000, v171
	v_lshlrev_b32_e32 v82, 16, v172
	v_and_b32_e32 v83, 0xffff0000, v172
	v_lshlrev_b32_e32 v68, 16, v173
	v_and_b32_e32 v69, 0xffff0000, v173
	s_waitcnt vmcnt(8)
	v_lshlrev_b32_e32 v84, 16, v174
	v_and_b32_e32 v85, 0xffff0000, v174
	v_lshlrev_b32_e32 v70, 16, v175
	v_and_b32_e32 v71, 0xffff0000, v175
	v_lshlrev_b32_e32 v86, 16, v176
	v_and_b32_e32 v87, 0xffff0000, v176
	v_lshlrev_b32_e32 v72, 16, v177
	v_and_b32_e32 v73, 0xffff0000, v177
	v_pk_fma_f32 v[62:63], v[80:81], s[26:27], v[62:63] op_sel_hi:[1,0,1]
	v_pk_fma_f32 v[64:65], v[66:67], s[26:27], v[64:65] op_sel_hi:[1,0,1]
	v_pk_fma_f32 v[58:59], v[82:83], s[26:27], v[58:59] op_sel_hi:[1,0,1]
	v_pk_fma_f32 v[60:61], v[68:69], s[26:27], v[60:61] op_sel_hi:[1,0,1]
	v_pk_fma_f32 v[54:55], v[84:85], s[26:27], v[54:55] op_sel_hi:[1,0,1]
	v_pk_fma_f32 v[56:57], v[70:71], s[26:27], v[56:57] op_sel_hi:[1,0,1]
	v_pk_fma_f32 v[66:67], v[86:87], s[26:27], v[50:51] op_sel_hi:[1,0,1]
	v_pk_fma_f32 v[68:69], v[72:73], s[26:27], v[52:53] op_sel_hi:[1,0,1]
	v_cvt_pk_bf16_f32 v50, v62, v63
	v_cvt_pk_bf16_f32 v51, v64, v65
	v_cvt_pk_bf16_f32 v52, v58, v59
	v_cvt_pk_bf16_f32 v53, v60, v61
	v_cvt_pk_bf16_f32 v54, v54, v55
	v_cvt_pk_bf16_f32 v55, v56, v57
	v_cvt_pk_bf16_f32 v56, v66, v67
	v_cvt_pk_bf16_f32 v57, v68, v69
	global_store_dwordx4 v[76:77], v[50:53], off
	global_store_dwordx4 v[76:77], v[54:57], off offset:256
	v_add_u32_e32 v170, 0xb0000, v146
	global_load_dwordx4 v[170:173], v170, s[12:13]
	v_add_u32_e32 v174, 0xb0000, v146
	global_load_dwordx4 v[174:177], v174, s[12:13] offset:256
	v_lshl_add_u64 v[58:59], v[146:147], 0, s[8:9]
	v_lshl_add_u64 v[60:61], s[14:15], 0, v[74:75]
	v_lshl_add_u64 v[62:63], s[12:13], 0, v[58:59]
	s_mov_b64 s[8:9], 0xb0000
	s_waitcnt vmcnt(8)
	v_lshlrev_b32_e32 v64, 16, v178
	v_and_b32_e32 v65, 0xffff0000, v178
	v_lshlrev_b32_e32 v50, 16, v179
	v_and_b32_e32 v51, 0xffff0000, v179
	v_lshlrev_b32_e32 v66, 16, v180
	v_and_b32_e32 v67, 0xffff0000, v180
	v_lshlrev_b32_e32 v52, 16, v181
	v_and_b32_e32 v53, 0xffff0000, v181
	s_waitcnt vmcnt(8)
	v_lshlrev_b32_e32 v68, 16, v182
	v_and_b32_e32 v69, 0xffff0000, v182
	v_lshlrev_b32_e32 v54, 16, v183
	v_and_b32_e32 v55, 0xffff0000, v183
	v_lshlrev_b32_e32 v70, 16, v184
	v_and_b32_e32 v71, 0xffff0000, v184
	v_lshlrev_b32_e32 v56, 16, v185
	v_and_b32_e32 v57, 0xffff0000, v185
	v_pk_fma_f32 v[46:47], v[64:65], s[26:27], v[46:47] op_sel_hi:[1,0,1]
	v_pk_fma_f32 v[48:49], v[50:51], s[26:27], v[48:49] op_sel_hi:[1,0,1]
	v_pk_fma_f32 v[42:43], v[66:67], s[26:27], v[42:43] op_sel_hi:[1,0,1]
	v_pk_fma_f32 v[44:45], v[52:53], s[26:27], v[44:45] op_sel_hi:[1,0,1]
	v_pk_fma_f32 v[38:39], v[68:69], s[26:27], v[38:39] op_sel_hi:[1,0,1]
	v_pk_fma_f32 v[40:41], v[54:55], s[26:27], v[40:41] op_sel_hi:[1,0,1]
	v_pk_fma_f32 v[50:51], v[70:71], s[26:27], v[34:35] op_sel_hi:[1,0,1]
	v_pk_fma_f32 v[52:53], v[56:57], s[26:27], v[36:37] op_sel_hi:[1,0,1]
	v_cvt_pk_bf16_f32 v34, v46, v47
	v_cvt_pk_bf16_f32 v35, v48, v49
	v_cvt_pk_bf16_f32 v36, v42, v43
	v_cvt_pk_bf16_f32 v37, v44, v45
	v_cvt_pk_bf16_f32 v38, v38, v39
	v_cvt_pk_bf16_f32 v39, v40, v41
	v_cvt_pk_bf16_f32 v40, v50, v51
	v_cvt_pk_bf16_f32 v41, v52, v53
	global_store_dwordx4 v[60:61], v[34:37], off
	global_store_dwordx4 v[60:61], v[38:41], off offset:256
	v_lshl_add_u64 v[42:43], v[146:147], 0, s[8:9]
	v_lshl_add_u64 v[44:45], s[14:15], 0, v[58:59]
	v_lshl_add_u64 v[46:47], s[12:13], 0, v[42:43]
	s_waitcnt vmcnt(6)
	v_lshlrev_b32_e32 v48, 16, v186
	v_and_b32_e32 v49, 0xffff0000, v186
	v_lshlrev_b32_e32 v34, 16, v187
	v_and_b32_e32 v35, 0xffff0000, v187
	v_lshlrev_b32_e32 v50, 16, v188
	v_and_b32_e32 v51, 0xffff0000, v188
	v_lshlrev_b32_e32 v36, 16, v189
	v_and_b32_e32 v37, 0xffff0000, v189
	s_waitcnt vmcnt(6)
	v_lshlrev_b32_e32 v52, 16, v190
	v_and_b32_e32 v53, 0xffff0000, v190
	v_lshlrev_b32_e32 v38, 16, v191
	v_and_b32_e32 v39, 0xffff0000, v191
	v_lshlrev_b32_e32 v54, 16, v192
	v_and_b32_e32 v55, 0xffff0000, v192
	v_lshlrev_b32_e32 v40, 16, v193
	v_and_b32_e32 v41, 0xffff0000, v193
	v_pk_fma_f32 v[30:31], v[48:49], s[26:27], v[30:31] op_sel_hi:[1,0,1]
	v_pk_fma_f32 v[32:33], v[34:35], s[26:27], v[32:33] op_sel_hi:[1,0,1]
	v_pk_fma_f32 v[26:27], v[50:51], s[26:27], v[26:27] op_sel_hi:[1,0,1]
	v_pk_fma_f32 v[28:29], v[36:37], s[26:27], v[28:29] op_sel_hi:[1,0,1]
	v_pk_fma_f32 v[22:23], v[52:53], s[26:27], v[22:23] op_sel_hi:[1,0,1]
	v_pk_fma_f32 v[24:25], v[38:39], s[26:27], v[24:25] op_sel_hi:[1,0,1]
	v_pk_fma_f32 v[34:35], v[54:55], s[26:27], v[18:19] op_sel_hi:[1,0,1]
	v_pk_fma_f32 v[36:37], v[40:41], s[26:27], v[20:21] op_sel_hi:[1,0,1]
	v_cvt_pk_bf16_f32 v18, v30, v31
	v_cvt_pk_bf16_f32 v19, v32, v33
	v_cvt_pk_bf16_f32 v20, v26, v27
	v_cvt_pk_bf16_f32 v21, v28, v29
	v_cvt_pk_bf16_f32 v22, v22, v23
	v_cvt_pk_bf16_f32 v23, v24, v25
	v_cvt_pk_bf16_f32 v24, v34, v35
	v_cvt_pk_bf16_f32 v25, v36, v37
	global_store_dwordx4 v[44:45], v[18:21], off
	global_store_dwordx4 v[44:45], v[22:25], off offset:256
	v_lshl_add_u64 v[26:27], s[14:15], 0, v[42:43]
	s_waitcnt vmcnt(4)
	v_lshlrev_b32_e32 v28, 16, v170
	v_and_b32_e32 v29, 0xffff0000, v170
	v_lshlrev_b32_e32 v18, 16, v171
	v_and_b32_e32 v19, 0xffff0000, v171
	v_lshlrev_b32_e32 v30, 16, v172
	v_and_b32_e32 v31, 0xffff0000, v172
	v_lshlrev_b32_e32 v20, 16, v173
	v_and_b32_e32 v21, 0xffff0000, v173
	s_waitcnt vmcnt(4)
	v_lshlrev_b32_e32 v32, 16, v174
	v_and_b32_e32 v33, 0xffff0000, v174
	v_lshlrev_b32_e32 v22, 16, v175
	v_and_b32_e32 v23, 0xffff0000, v175
	v_lshlrev_b32_e32 v34, 16, v176
	v_and_b32_e32 v35, 0xffff0000, v176
	v_lshlrev_b32_e32 v24, 16, v177
	v_and_b32_e32 v25, 0xffff0000, v177
	v_pk_fma_f32 v[14:15], v[28:29], s[26:27], v[14:15] op_sel_hi:[1,0,1]
	v_pk_fma_f32 v[16:17], v[18:19], s[26:27], v[16:17] op_sel_hi:[1,0,1]
	v_pk_fma_f32 v[10:11], v[30:31], s[26:27], v[10:11] op_sel_hi:[1,0,1]
	v_pk_fma_f32 v[12:13], v[20:21], s[26:27], v[12:13] op_sel_hi:[1,0,1]
	v_pk_fma_f32 v[6:7], v[32:33], s[26:27], v[6:7] op_sel_hi:[1,0,1]
	v_pk_fma_f32 v[8:9], v[22:23], s[26:27], v[8:9] op_sel_hi:[1,0,1]
	v_pk_fma_f32 v[18:19], v[34:35], s[26:27], v[2:3] op_sel_hi:[1,0,1]
	v_pk_fma_f32 v[20:21], v[24:25], s[26:27], v[4:5] op_sel_hi:[1,0,1]
	v_cvt_pk_bf16_f32 v2, v14, v15
	v_cvt_pk_bf16_f32 v3, v16, v17
	v_cvt_pk_bf16_f32 v4, v10, v11
	v_cvt_pk_bf16_f32 v5, v12, v13
	v_cvt_pk_bf16_f32 v6, v6, v7
	v_cvt_pk_bf16_f32 v7, v8, v9
	v_cvt_pk_bf16_f32 v8, v18, v19
	v_cvt_pk_bf16_f32 v9, v20, v21
	global_store_dwordx4 v[26:27], v[2:5], off
	global_store_dwordx4 v[26:27], v[6:9], off offset:256
	s_cbranch_vccnz .LBB0_671
	s_andn2_b64 vcc, exec, s[10:11]
	s_cbranch_vccnz .LBB0_670
	s_barrier
	s_branch .LBB0_670
